# v12 + moe_rows gather of the up phases: all per-wave token-list loads issued back to back, one wait, then the LDS writes (was load-wait-write per iteration)
# speedup vs baseline: 1.0040x; 1.0040x over previous
; #define GAS __attribute__((address_space(1)))
; #define LAS __attribute__((address_space(3)))
; __device__ __forceinline__ void moe_rows(Frame& F, LAS int* rows, int NBr, int NBt, int NPN, const int* list, int cstart, bool UP_IDENT_ON = false) {
;     const LAS int* tb = (const LAS int*)(F.lds + TBL_OFF);
;     for (int idx = F.tid; idx < 16 * 256; idx += NWAVES * 64) { const int i = idx >> 8, r = idx & 255; const int L = i * F.G + F.vcu; if (L >= NBt * NPN) break;
;         const int blk = L / NPN; int tok;
;         if (blk < NBr) { const int w = tb[blk], e = w >> 16, pos = (w & 0xffff) * 256 + r; tok = pos < tb[1024 + 128 + e] ? ((const GAS int*)list)[(size_t)e * CAP + pos] : cstart; }
;         else tok = cstart + (blk - NBr) * 256 + r;
;     ...
;         if (UP_IDENT_ON) tok = cstart + ((i * 7 + (F.vcu & 63)) & 63) * 256 + r;
;     ...
;         rows[idx] = tok; }
;     __syncthreads();
; }
.LBB0_752:
	s_add_i32 s2, 0, 0x21500
	v_mov_b32_e32 v2, s2
	s_waitcnt lgkmcnt(0)
	s_barrier
	ds_read_b32 v2, v2
	s_movk_i32 s2, 0x1000
	s_mov_b64 s[38:39], s[12:13]
	v_cmp_gt_i32_e32 vcc, s2, v1
	s_waitcnt lgkmcnt(0)
	v_readfirstlane_b32 s9, v2
	s_lshl_b32 s22, s9, 1
	s_addk_i32 s22, 0x110
	s_and_saveexec_b64 s[2:3], vcc
	s_cbranch_execz .LBB0_763
	s_add_u32 s4, s12, 0x1500000
	s_addc_u32 s5, s13, 0
	s_add_i32 s23, 0, 0x20400
	s_mov_b32 s40, 0xffff00
	s_movk_i32 s41, 0xdff
	v_and_b32_e32 v4, 0xff, v1
	v_lshl_add_u32 v5, v1, 2, 0
	v_add_u32_e32 v5, 0x22000, v5
	v_mov_b32_e32 v3, 0
	v_ashrrev_i32_e32 v2, 8, v1
	v_mul_lo_u32 v2, v2, s67
	v_add_u32_e32 v2, s71, v2
	s_lshl_b32 s14, s67, 1
	v_readfirstlane_b32 s10, v2
	s_mov_b32 s11, s10
	v_mov_b32_e32 v10, 0
	s_cmp_ge_i32 s10, s22
	s_cbranch_scc1 .Lmra_ld_done
	s_lshr_b32 s15, s10, 1
	s_cmp_ge_i32 s15, s9
	s_cbranch_scc1 .Lmra_sh0
	s_lshl_b32 s16, s15, 2
	s_add_i32 s16, s16, 0x20400
	v_mov_b32_e32 v6, s16
	ds_read_b32 v6, v6
	s_waitcnt lgkmcnt(0)
	v_readfirstlane_b32 s16, v6
	s_ashr_i32 s17, s16, 16
	s_lshl_b32 s15, s17, 2
	s_add_i32 s15, s15, 0x21600
	v_mov_b32_e32 v7, s15
	ds_read_b32 v7, v7
	s_and_b32 s16, s16, 0xffff
	s_lshl_b32 s16, s16, 8
	v_or_b32_e32 v8, s16, v4
	s_mul_i32 s17, s17, 0x8800
	v_add_lshl_u32 v9, v8, s17, 2
	s_waitcnt lgkmcnt(0)
	v_cmp_lt_i32_e32 vcc, v8, v7
	s_and_saveexec_b64 s[18:19], vcc
	global_load_dword v10, v9, s[4:5]
	s_or_b64 exec, exec, s[18:19]
	s_branch .Lmra_nx0
.Lmra_sh0:
	s_sub_i32 s16, s15, s9
	s_lshl_b32 s16, s16, 8
	v_or_b32_e32 v10, s16, v4
.Lmra_nx0:
	s_add_i32 s10, s10, s14
	v_mov_b32_e32 v11, 0
	s_cmp_ge_i32 s10, s22
	s_cbranch_scc1 .Lmra_ld_done
	s_lshr_b32 s15, s10, 1
	s_cmp_ge_i32 s15, s9
	s_cbranch_scc1 .Lmra_sh1
	s_lshl_b32 s16, s15, 2
	s_add_i32 s16, s16, 0x20400
	v_mov_b32_e32 v6, s16
	ds_read_b32 v6, v6
	s_waitcnt lgkmcnt(0)
	v_readfirstlane_b32 s16, v6
	s_ashr_i32 s17, s16, 16
	s_lshl_b32 s15, s17, 2
	s_add_i32 s15, s15, 0x21600
	v_mov_b32_e32 v7, s15
	ds_read_b32 v7, v7
	s_and_b32 s16, s16, 0xffff
	s_lshl_b32 s16, s16, 8
	v_or_b32_e32 v8, s16, v4
	s_mul_i32 s17, s17, 0x8800
	v_add_lshl_u32 v9, v8, s17, 2
	s_waitcnt lgkmcnt(0)
	v_cmp_lt_i32_e32 vcc, v8, v7
	s_and_saveexec_b64 s[18:19], vcc
	global_load_dword v11, v9, s[4:5]
	s_or_b64 exec, exec, s[18:19]
	s_branch .Lmra_nx1
.Lmra_sh1:
	s_sub_i32 s16, s15, s9
	s_lshl_b32 s16, s16, 8
	v_or_b32_e32 v11, s16, v4
.Lmra_nx1:
	s_add_i32 s10, s10, s14
	v_mov_b32_e32 v12, 0
	s_cmp_ge_i32 s10, s22
	s_cbranch_scc1 .Lmra_ld_done
	s_lshr_b32 s15, s10, 1
	s_cmp_ge_i32 s15, s9
	s_cbranch_scc1 .Lmra_sh2
	s_lshl_b32 s16, s15, 2
	s_add_i32 s16, s16, 0x20400
	v_mov_b32_e32 v6, s16
	ds_read_b32 v6, v6
	s_waitcnt lgkmcnt(0)
	v_readfirstlane_b32 s16, v6
	s_ashr_i32 s17, s16, 16
	s_lshl_b32 s15, s17, 2
	s_add_i32 s15, s15, 0x21600
	v_mov_b32_e32 v7, s15
	ds_read_b32 v7, v7
	s_and_b32 s16, s16, 0xffff
	s_lshl_b32 s16, s16, 8
	v_or_b32_e32 v8, s16, v4
	s_mul_i32 s17, s17, 0x8800
	v_add_lshl_u32 v9, v8, s17, 2
	s_waitcnt lgkmcnt(0)
	v_cmp_lt_i32_e32 vcc, v8, v7
	s_and_saveexec_b64 s[18:19], vcc
	global_load_dword v12, v9, s[4:5]
	s_or_b64 exec, exec, s[18:19]
	s_branch .Lmra_nx2
.Lmra_sh2:
	s_sub_i32 s16, s15, s9
	s_lshl_b32 s16, s16, 8
	v_or_b32_e32 v12, s16, v4
.Lmra_nx2:
	s_add_i32 s10, s10, s14
	v_mov_b32_e32 v13, 0
	s_cmp_ge_i32 s10, s22
	s_cbranch_scc1 .Lmra_ld_done
	s_lshr_b32 s15, s10, 1
	s_cmp_ge_i32 s15, s9
	s_cbranch_scc1 .Lmra_sh3
	s_lshl_b32 s16, s15, 2
	s_add_i32 s16, s16, 0x20400
	v_mov_b32_e32 v6, s16
	ds_read_b32 v6, v6
	s_waitcnt lgkmcnt(0)
	v_readfirstlane_b32 s16, v6
	s_ashr_i32 s17, s16, 16
	s_lshl_b32 s15, s17, 2
	s_add_i32 s15, s15, 0x21600
	v_mov_b32_e32 v7, s15
	ds_read_b32 v7, v7
	s_and_b32 s16, s16, 0xffff
	s_lshl_b32 s16, s16, 8
	v_or_b32_e32 v8, s16, v4
	s_mul_i32 s17, s17, 0x8800
	v_add_lshl_u32 v9, v8, s17, 2
	s_waitcnt lgkmcnt(0)
	v_cmp_lt_i32_e32 vcc, v8, v7
	s_and_saveexec_b64 s[18:19], vcc
	global_load_dword v13, v9, s[4:5]
	s_or_b64 exec, exec, s[18:19]
	s_branch .Lmra_nx3
.Lmra_sh3:
	s_sub_i32 s16, s15, s9
	s_lshl_b32 s16, s16, 8
	v_or_b32_e32 v13, s16, v4
; #define GAS __attribute__((address_space(1)))
; #define LAS __attribute__((address_space(3)))
;     __device__ __forceinline__ bool next(int i, pg8::Unit& u) const {
;         const int L = i * G + vcu; if (L >= NBt * NPN) return false;
;         const int blk = L / NPN, pn = L - blk * NPN; u.pm = blk; u.pn = pn;
;         if (blk < NBr) { const int w = tb[blk]; u.aux = GATHER ? i : w; u.B = Bexp + (unsigned)(w >> 16) * bstride + (unsigned)pn * 256u * ldb * 2u; }
;         else { u.aux = GATHER ? i : -1; u.B = Bsh + (unsigned)pn * 256u * ldb * 2u; }
;         u.A = GATHER ? Asrc : Asrc + (unsigned)blk * 256u * lda * 2u; return true;
; __device__ __forceinline__ void moe_rows(Frame& F, LAS int* rows, int NBr, int NBt, int NPN, const int* list, int cstart, bool UP_IDENT_ON = false) {
;     const LAS int* tb = (const LAS int*)(F.lds + TBL_OFF);
;     for (int idx = F.tid; idx < 16 * 256; idx += NWAVES * 64) { const int i = idx >> 8, r = idx & 255; const int L = i * F.G + F.vcu; if (L >= NBt * NPN) break;
;         const int blk = L / NPN; int tok;
;         if (blk < NBr) { const int w = tb[blk], e = w >> 16, pos = (w & 0xffff) * 256 + r; tok = pos < tb[1024 + 128 + e] ? ((const GAS int*)list)[(size_t)e * CAP + pos] : cstart; }
;         else tok = cstart + (blk - NBr) * 256 + r;
;     ...
;         if (UP_IDENT_ON) tok = cstart + ((i * 7 + (F.vcu & 63)) & 63) * 256 + r;
;     ...
;         rows[idx] = tok; }
;     __syncthreads();
; }
.Lmra_nx3:
	s_add_i32 s10, s10, s14
	v_mov_b32_e32 v14, 0
	s_cmp_ge_i32 s10, s22
	s_cbranch_scc1 .Lmra_ld_done
	s_lshr_b32 s15, s10, 1
	s_cmp_ge_i32 s15, s9
	s_cbranch_scc1 .Lmra_sh4
	s_lshl_b32 s16, s15, 2
	s_add_i32 s16, s16, 0x20400
	v_mov_b32_e32 v6, s16
	ds_read_b32 v6, v6
	s_waitcnt lgkmcnt(0)
	v_readfirstlane_b32 s16, v6
	s_ashr_i32 s17, s16, 16
	s_lshl_b32 s15, s17, 2
	s_add_i32 s15, s15, 0x21600
	v_mov_b32_e32 v7, s15
	ds_read_b32 v7, v7
	s_and_b32 s16, s16, 0xffff
	s_lshl_b32 s16, s16, 8
	v_or_b32_e32 v8, s16, v4
	s_mul_i32 s17, s17, 0x8800
	v_add_lshl_u32 v9, v8, s17, 2
	s_waitcnt lgkmcnt(0)
	v_cmp_lt_i32_e32 vcc, v8, v7
	s_and_saveexec_b64 s[18:19], vcc
	global_load_dword v14, v9, s[4:5]
	s_or_b64 exec, exec, s[18:19]
	s_branch .Lmra_nx4
.Lmra_sh4:
	s_sub_i32 s16, s15, s9
	s_lshl_b32 s16, s16, 8
	v_or_b32_e32 v14, s16, v4
.Lmra_nx4:
	s_add_i32 s10, s10, s14
	v_mov_b32_e32 v15, 0
	s_cmp_ge_i32 s10, s22
	s_cbranch_scc1 .Lmra_ld_done
	s_lshr_b32 s15, s10, 1
	s_cmp_ge_i32 s15, s9
	s_cbranch_scc1 .Lmra_sh5
	s_lshl_b32 s16, s15, 2
	s_add_i32 s16, s16, 0x20400
	v_mov_b32_e32 v6, s16
	ds_read_b32 v6, v6
	s_waitcnt lgkmcnt(0)
	v_readfirstlane_b32 s16, v6
	s_ashr_i32 s17, s16, 16
	s_lshl_b32 s15, s17, 2
	s_add_i32 s15, s15, 0x21600
	v_mov_b32_e32 v7, s15
	ds_read_b32 v7, v7
	s_and_b32 s16, s16, 0xffff
	s_lshl_b32 s16, s16, 8
	v_or_b32_e32 v8, s16, v4
	s_mul_i32 s17, s17, 0x8800
	v_add_lshl_u32 v9, v8, s17, 2
	s_waitcnt lgkmcnt(0)
	v_cmp_lt_i32_e32 vcc, v8, v7
	s_and_saveexec_b64 s[18:19], vcc
	global_load_dword v15, v9, s[4:5]
	s_or_b64 exec, exec, s[18:19]
	s_branch .Lmra_nx5
.Lmra_sh5:
	s_sub_i32 s16, s15, s9
	s_lshl_b32 s16, s16, 8
	v_or_b32_e32 v15, s16, v4
.Lmra_nx5:
	s_add_i32 s10, s10, s14
	v_mov_b32_e32 v16, 0
	s_cmp_ge_i32 s10, s22
	s_cbranch_scc1 .Lmra_ld_done
	s_lshr_b32 s15, s10, 1
	s_cmp_ge_i32 s15, s9
	s_cbranch_scc1 .Lmra_sh6
	s_lshl_b32 s16, s15, 2
	s_add_i32 s16, s16, 0x20400
	v_mov_b32_e32 v6, s16
	ds_read_b32 v6, v6
	s_waitcnt lgkmcnt(0)
	v_readfirstlane_b32 s16, v6
	s_ashr_i32 s17, s16, 16
	s_lshl_b32 s15, s17, 2
	s_add_i32 s15, s15, 0x21600
	v_mov_b32_e32 v7, s15
	ds_read_b32 v7, v7
	s_and_b32 s16, s16, 0xffff
	s_lshl_b32 s16, s16, 8
	v_or_b32_e32 v8, s16, v4
	s_mul_i32 s17, s17, 0x8800
	v_add_lshl_u32 v9, v8, s17, 2
	s_waitcnt lgkmcnt(0)
	v_cmp_lt_i32_e32 vcc, v8, v7
	s_and_saveexec_b64 s[18:19], vcc
	global_load_dword v16, v9, s[4:5]
	s_or_b64 exec, exec, s[18:19]
	s_branch .Lmra_nx6
.Lmra_sh6:
	s_sub_i32 s16, s15, s9
	s_lshl_b32 s16, s16, 8
	v_or_b32_e32 v16, s16, v4
.Lmra_nx6:
	s_add_i32 s10, s10, s14
	v_mov_b32_e32 v17, 0
	s_cmp_ge_i32 s10, s22
	s_cbranch_scc1 .Lmra_ld_done
	s_lshr_b32 s15, s10, 1
	s_cmp_ge_i32 s15, s9
	s_cbranch_scc1 .Lmra_sh7
	s_lshl_b32 s16, s15, 2
	s_add_i32 s16, s16, 0x20400
	v_mov_b32_e32 v6, s16
	ds_read_b32 v6, v6
	s_waitcnt lgkmcnt(0)
	v_readfirstlane_b32 s16, v6
	s_ashr_i32 s17, s16, 16
	s_lshl_b32 s15, s17, 2
	s_add_i32 s15, s15, 0x21600
	v_mov_b32_e32 v7, s15
	ds_read_b32 v7, v7
	s_and_b32 s16, s16, 0xffff
	s_lshl_b32 s16, s16, 8
	v_or_b32_e32 v8, s16, v4
	s_mul_i32 s17, s17, 0x8800
	v_add_lshl_u32 v9, v8, s17, 2
	s_waitcnt lgkmcnt(0)
	v_cmp_lt_i32_e32 vcc, v8, v7
	s_and_saveexec_b64 s[18:19], vcc
	global_load_dword v17, v9, s[4:5]
	s_or_b64 exec, exec, s[18:19]
	s_branch .Lmra_nx7
.Lmra_sh7:
	s_sub_i32 s16, s15, s9
	s_lshl_b32 s16, s16, 8
	v_or_b32_e32 v17, s16, v4
.Lmra_nx7:
	s_add_i32 s10, s10, s14
.Lmra_ld_done:
	s_waitcnt vmcnt(0)
	s_cmp_ge_i32 s11, s22
	s_cbranch_scc1 .Lmra_wr_done
	ds_write_b32 v5, v10
	s_add_i32 s11, s11, s14
	s_cmp_ge_i32 s11, s22
	s_cbranch_scc1 .Lmra_wr_done
	ds_write_b32 v5, v11 offset:2048
	s_add_i32 s11, s11, s14
	s_cmp_ge_i32 s11, s22
	s_cbranch_scc1 .Lmra_wr_done
	ds_write_b32 v5, v12 offset:4096
	s_add_i32 s11, s11, s14
	s_cmp_ge_i32 s11, s22
	s_cbranch_scc1 .Lmra_wr_done
	ds_write_b32 v5, v13 offset:6144
	s_add_i32 s11, s11, s14
	s_cmp_ge_i32 s11, s22
	s_cbranch_scc1 .Lmra_wr_done
	ds_write_b32 v5, v14 offset:8192
	s_add_i32 s11, s11, s14
	s_cmp_ge_i32 s11, s22
	s_cbranch_scc1 .Lmra_wr_done
	ds_write_b32 v5, v15 offset:10240
	s_add_i32 s11, s11, s14
	s_cmp_ge_i32 s11, s22
	s_cbranch_scc1 .Lmra_wr_done
	ds_write_b32 v5, v16 offset:12288
	s_add_i32 s11, s11, s14
	s_cmp_ge_i32 s11, s22
	s_cbranch_scc1 .Lmra_wr_done
	ds_write_b32 v5, v17 offset:14336
	s_add_i32 s11, s11, s14
.Lmra_wr_done:
.LBB0_763:
	s_or_b64 exec, exec, s[2:3]
	v_mov_b32_e32 v2, v0
	s_waitcnt lgkmcnt(0)
	s_barrier
	s_cmp_ge_i32 s71, s22
	v_readfirstlane_b32 s10, v2
	s_cbranch_scc1 .LBB0_789
	s_lshr_b32 s2, s71, 31
	s_add_i32 s2, s71, s2
	s_ashr_i32 s59, s2, 1
	s_and_b32 s2, s2, -2
	s_sub_i32 s58, s71, s2
	s_cmp_ge_i32 s59, s9
	s_cbranch_scc0 .LBB0_766
	s_lshl_b32 s2, s58, 19
	s_add_i32 s60, s2, 0x1100000
	s_cbranch_execz .LBB0_767
	s_branch .LBB0_768

; #define GAS __attribute__((address_space(1)))
; #define LAS __attribute__((address_space(3)))
; __device__ __forceinline__ void moe_rows(Frame& F, LAS int* rows, int NBr, int NBt, int NPN, const int* list, int cstart, bool UP_IDENT_ON = false) {
;     const LAS int* tb = (const LAS int*)(F.lds + TBL_OFF);
;     for (int idx = F.tid; idx < 16 * 256; idx += NWAVES * 64) { const int i = idx >> 8, r = idx & 255; const int L = i * F.G + F.vcu; if (L >= NBt * NPN) break;
;         const int blk = L / NPN; int tok;
;         if (blk < NBr) { const int w = tb[blk], e = w >> 16, pos = (w & 0xffff) * 256 + r; tok = pos < tb[1024 + 128 + e] ? ((const GAS int*)list)[(size_t)e * CAP + pos] : cstart; }
;         else tok = cstart + (blk - NBr) * 256 + r;
;     ...
;         if (UP_IDENT_ON) tok = cstart + ((i * 7 + (F.vcu & 63)) & 63) * 256 + r;
;     ...
;         rows[idx] = tok; }
;     __syncthreads();
; }
.LBB0_1604:
	s_add_i32 s2, 0, 0x21500
	v_mov_b32_e32 v2, s2
	s_waitcnt lgkmcnt(0)
	s_barrier
	ds_read_b32 v2, v2
	s_movk_i32 s2, 0x1000
	s_mov_b64 s[38:39], s[8:9]
	v_cmp_gt_i32_e32 vcc, s2, v1
	s_waitcnt lgkmcnt(0)
	v_readfirstlane_b32 s20, v2
	s_lshl_b32 s21, s20, 1
	s_addk_i32 s21, 0x100
	s_and_saveexec_b64 s[2:3], vcc
	s_cbranch_execz .LBB0_1615
	s_add_u32 s4, s8, 0x1500000
	s_addc_u32 s5, s9, 0
	s_add_i32 s22, 0, 0x20400
	s_mov_b32 s23, 0xffff00
	s_movk_i32 s40, 0xdff
	v_and_b32_e32 v4, 0xff, v1
	v_lshl_add_u32 v5, v1, 2, 0
	v_add_u32_e32 v5, 0x22000, v5
	v_mov_b32_e32 v3, 0
	v_ashrrev_i32_e32 v2, 8, v1
	v_mul_lo_u32 v2, v2, s67
	v_add_u32_e32 v2, s71, v2
	s_lshl_b32 s12, s67, 1
	v_readfirstlane_b32 s10, v2
	s_mov_b32 s11, s10
	v_mov_b32_e32 v10, 0
	s_cmp_ge_i32 s10, s21
	s_cbranch_scc1 .Lmrb_ld_done
	s_lshr_b32 s13, s10, 1
	s_cmp_ge_i32 s13, s20
	s_cbranch_scc1 .Lmrb_sh0
	s_lshl_b32 s14, s13, 2
	s_add_i32 s14, s14, 0x20400
	v_mov_b32_e32 v6, s14
	ds_read_b32 v6, v6
	s_waitcnt lgkmcnt(0)
	v_readfirstlane_b32 s14, v6
	s_ashr_i32 s15, s14, 16
	s_lshl_b32 s13, s15, 2
	s_add_i32 s13, s13, 0x21600
	v_mov_b32_e32 v7, s13
	ds_read_b32 v7, v7
	s_and_b32 s14, s14, 0xffff
	s_lshl_b32 s14, s14, 8
	v_or_b32_e32 v8, s14, v4
	s_mul_i32 s15, s15, 0x8800
	v_add_lshl_u32 v9, v8, s15, 2
	s_waitcnt lgkmcnt(0)
	v_cmp_lt_i32_e32 vcc, v8, v7
	s_and_saveexec_b64 s[16:17], vcc
	global_load_dword v10, v9, s[4:5]
	s_or_b64 exec, exec, s[16:17]
	s_branch .Lmrb_nx0
.Lmrb_sh0:
	s_sub_i32 s14, s13, s20
	s_lshl_b32 s14, s14, 8
	v_or_b32_e32 v10, s14, v4
.Lmrb_nx0:
	s_add_i32 s10, s10, s12
	v_mov_b32_e32 v11, 0
	s_cmp_ge_i32 s10, s21
	s_cbranch_scc1 .Lmrb_ld_done
	s_lshr_b32 s13, s10, 1
	s_cmp_ge_i32 s13, s20
	s_cbranch_scc1 .Lmrb_sh1
	s_lshl_b32 s14, s13, 2
	s_add_i32 s14, s14, 0x20400
	v_mov_b32_e32 v6, s14
	ds_read_b32 v6, v6
	s_waitcnt lgkmcnt(0)
	v_readfirstlane_b32 s14, v6
	s_ashr_i32 s15, s14, 16
	s_lshl_b32 s13, s15, 2
	s_add_i32 s13, s13, 0x21600
	v_mov_b32_e32 v7, s13
	ds_read_b32 v7, v7
	s_and_b32 s14, s14, 0xffff
	s_lshl_b32 s14, s14, 8
	v_or_b32_e32 v8, s14, v4
	s_mul_i32 s15, s15, 0x8800
	v_add_lshl_u32 v9, v8, s15, 2
	s_waitcnt lgkmcnt(0)
	v_cmp_lt_i32_e32 vcc, v8, v7
	s_and_saveexec_b64 s[16:17], vcc
	global_load_dword v11, v9, s[4:5]
	s_or_b64 exec, exec, s[16:17]
	s_branch .Lmrb_nx1
.Lmrb_sh1:
	s_sub_i32 s14, s13, s20
	s_lshl_b32 s14, s14, 8
	v_or_b32_e32 v11, s14, v4
.Lmrb_nx1:
	s_add_i32 s10, s10, s12
	v_mov_b32_e32 v12, 0
	s_cmp_ge_i32 s10, s21
	s_cbranch_scc1 .Lmrb_ld_done
	s_lshr_b32 s13, s10, 1
	s_cmp_ge_i32 s13, s20
	s_cbranch_scc1 .Lmrb_sh2
	s_lshl_b32 s14, s13, 2
	s_add_i32 s14, s14, 0x20400
	v_mov_b32_e32 v6, s14
	ds_read_b32 v6, v6
	s_waitcnt lgkmcnt(0)
	v_readfirstlane_b32 s14, v6
	s_ashr_i32 s15, s14, 16
	s_lshl_b32 s13, s15, 2
	s_add_i32 s13, s13, 0x21600
	v_mov_b32_e32 v7, s13
	ds_read_b32 v7, v7
	s_and_b32 s14, s14, 0xffff
	s_lshl_b32 s14, s14, 8
	v_or_b32_e32 v8, s14, v4
	s_mul_i32 s15, s15, 0x8800
	v_add_lshl_u32 v9, v8, s15, 2
	s_waitcnt lgkmcnt(0)
	v_cmp_lt_i32_e32 vcc, v8, v7
	s_and_saveexec_b64 s[16:17], vcc
	global_load_dword v12, v9, s[4:5]
	s_or_b64 exec, exec, s[16:17]
	s_branch .Lmrb_nx2
.Lmrb_sh2:
	s_sub_i32 s14, s13, s20
	s_lshl_b32 s14, s14, 8
	v_or_b32_e32 v12, s14, v4
.Lmrb_nx2:
	s_add_i32 s10, s10, s12
	v_mov_b32_e32 v13, 0
	s_cmp_ge_i32 s10, s21
	s_cbranch_scc1 .Lmrb_ld_done
	s_lshr_b32 s13, s10, 1
	s_cmp_ge_i32 s13, s20
	s_cbranch_scc1 .Lmrb_sh3
	s_lshl_b32 s14, s13, 2
	s_add_i32 s14, s14, 0x20400
	v_mov_b32_e32 v6, s14
	ds_read_b32 v6, v6
	s_waitcnt lgkmcnt(0)
	v_readfirstlane_b32 s14, v6
	s_ashr_i32 s15, s14, 16
	s_lshl_b32 s13, s15, 2
	s_add_i32 s13, s13, 0x21600
	v_mov_b32_e32 v7, s13
	ds_read_b32 v7, v7
	s_and_b32 s14, s14, 0xffff
	s_lshl_b32 s14, s14, 8
	v_or_b32_e32 v8, s14, v4
	s_mul_i32 s15, s15, 0x8800
	v_add_lshl_u32 v9, v8, s15, 2
	s_waitcnt lgkmcnt(0)
	v_cmp_lt_i32_e32 vcc, v8, v7
	s_and_saveexec_b64 s[16:17], vcc
	global_load_dword v13, v9, s[4:5]
	s_or_b64 exec, exec, s[16:17]
	s_branch .Lmrb_nx3
.Lmrb_sh3:
	s_sub_i32 s14, s13, s20
	s_lshl_b32 s14, s14, 8
	v_or_b32_e32 v13, s14, v4
; #define GAS __attribute__((address_space(1)))
; #define LAS __attribute__((address_space(3)))
;     __device__ __forceinline__ bool next(int i, pg8::Unit& u) const {
;         const int L = i * G + vcu; if (L >= NBt * NPN) return false;
;         const int blk = L / NPN, pn = L - blk * NPN; u.pm = blk; u.pn = pn;
;         if (blk < NBr) { const int w = tb[blk]; u.aux = GATHER ? i : w; u.B = Bexp + (unsigned)(w >> 16) * bstride + (unsigned)pn * 256u * ldb * 2u; }
;         else { u.aux = GATHER ? i : -1; u.B = Bsh + (unsigned)pn * 256u * ldb * 2u; }
;         u.A = GATHER ? Asrc : Asrc + (unsigned)blk * 256u * lda * 2u; return true;
; __device__ __forceinline__ void moe_rows(Frame& F, LAS int* rows, int NBr, int NBt, int NPN, const int* list, int cstart, bool UP_IDENT_ON = false) {
;     const LAS int* tb = (const LAS int*)(F.lds + TBL_OFF);
;     for (int idx = F.tid; idx < 16 * 256; idx += NWAVES * 64) { const int i = idx >> 8, r = idx & 255; const int L = i * F.G + F.vcu; if (L >= NBt * NPN) break;
;         const int blk = L / NPN; int tok;
;         if (blk < NBr) { const int w = tb[blk], e = w >> 16, pos = (w & 0xffff) * 256 + r; tok = pos < tb[1024 + 128 + e] ? ((const GAS int*)list)[(size_t)e * CAP + pos] : cstart; }
;         else tok = cstart + (blk - NBr) * 256 + r;
;     ...
;         if (UP_IDENT_ON) tok = cstart + ((i * 7 + (F.vcu & 63)) & 63) * 256 + r;
;     ...
;         rows[idx] = tok; }
;     __syncthreads();
; }
.Lmrb_nx3:
	s_add_i32 s10, s10, s12
	v_mov_b32_e32 v14, 0
	s_cmp_ge_i32 s10, s21
	s_cbranch_scc1 .Lmrb_ld_done
	s_lshr_b32 s13, s10, 1
	s_cmp_ge_i32 s13, s20
	s_cbranch_scc1 .Lmrb_sh4
	s_lshl_b32 s14, s13, 2
	s_add_i32 s14, s14, 0x20400
	v_mov_b32_e32 v6, s14
	ds_read_b32 v6, v6
	s_waitcnt lgkmcnt(0)
	v_readfirstlane_b32 s14, v6
	s_ashr_i32 s15, s14, 16
	s_lshl_b32 s13, s15, 2
	s_add_i32 s13, s13, 0x21600
	v_mov_b32_e32 v7, s13
	ds_read_b32 v7, v7
	s_and_b32 s14, s14, 0xffff
	s_lshl_b32 s14, s14, 8
	v_or_b32_e32 v8, s14, v4
	s_mul_i32 s15, s15, 0x8800
	v_add_lshl_u32 v9, v8, s15, 2
	s_waitcnt lgkmcnt(0)
	v_cmp_lt_i32_e32 vcc, v8, v7
	s_and_saveexec_b64 s[16:17], vcc
	global_load_dword v14, v9, s[4:5]
	s_or_b64 exec, exec, s[16:17]
	s_branch .Lmrb_nx4
.Lmrb_sh4:
	s_sub_i32 s14, s13, s20
	s_lshl_b32 s14, s14, 8
	v_or_b32_e32 v14, s14, v4
.Lmrb_nx4:
	s_add_i32 s10, s10, s12
	v_mov_b32_e32 v15, 0
	s_cmp_ge_i32 s10, s21
	s_cbranch_scc1 .Lmrb_ld_done
	s_lshr_b32 s13, s10, 1
	s_cmp_ge_i32 s13, s20
	s_cbranch_scc1 .Lmrb_sh5
	s_lshl_b32 s14, s13, 2
	s_add_i32 s14, s14, 0x20400
	v_mov_b32_e32 v6, s14
	ds_read_b32 v6, v6
	s_waitcnt lgkmcnt(0)
	v_readfirstlane_b32 s14, v6
	s_ashr_i32 s15, s14, 16
	s_lshl_b32 s13, s15, 2
	s_add_i32 s13, s13, 0x21600
	v_mov_b32_e32 v7, s13
	ds_read_b32 v7, v7
	s_and_b32 s14, s14, 0xffff
	s_lshl_b32 s14, s14, 8
	v_or_b32_e32 v8, s14, v4
	s_mul_i32 s15, s15, 0x8800
	v_add_lshl_u32 v9, v8, s15, 2
	s_waitcnt lgkmcnt(0)
	v_cmp_lt_i32_e32 vcc, v8, v7
	s_and_saveexec_b64 s[16:17], vcc
	global_load_dword v15, v9, s[4:5]
	s_or_b64 exec, exec, s[16:17]
	s_branch .Lmrb_nx5
.Lmrb_sh5:
	s_sub_i32 s14, s13, s20
	s_lshl_b32 s14, s14, 8
	v_or_b32_e32 v15, s14, v4
.Lmrb_nx5:
	s_add_i32 s10, s10, s12
	v_mov_b32_e32 v16, 0
	s_cmp_ge_i32 s10, s21
	s_cbranch_scc1 .Lmrb_ld_done
	s_lshr_b32 s13, s10, 1
	s_cmp_ge_i32 s13, s20
	s_cbranch_scc1 .Lmrb_sh6
	s_lshl_b32 s14, s13, 2
	s_add_i32 s14, s14, 0x20400
	v_mov_b32_e32 v6, s14
	ds_read_b32 v6, v6
	s_waitcnt lgkmcnt(0)
	v_readfirstlane_b32 s14, v6
	s_ashr_i32 s15, s14, 16
	s_lshl_b32 s13, s15, 2
	s_add_i32 s13, s13, 0x21600
	v_mov_b32_e32 v7, s13
	ds_read_b32 v7, v7
	s_and_b32 s14, s14, 0xffff
	s_lshl_b32 s14, s14, 8
	v_or_b32_e32 v8, s14, v4
	s_mul_i32 s15, s15, 0x8800
	v_add_lshl_u32 v9, v8, s15, 2
	s_waitcnt lgkmcnt(0)
	v_cmp_lt_i32_e32 vcc, v8, v7
	s_and_saveexec_b64 s[16:17], vcc
	global_load_dword v16, v9, s[4:5]
	s_or_b64 exec, exec, s[16:17]
	s_branch .Lmrb_nx6
.Lmrb_sh6:
	s_sub_i32 s14, s13, s20
	s_lshl_b32 s14, s14, 8
	v_or_b32_e32 v16, s14, v4
.Lmrb_nx6:
	s_add_i32 s10, s10, s12
	v_mov_b32_e32 v17, 0
	s_cmp_ge_i32 s10, s21
	s_cbranch_scc1 .Lmrb_ld_done
	s_lshr_b32 s13, s10, 1
	s_cmp_ge_i32 s13, s20
	s_cbranch_scc1 .Lmrb_sh7
	s_lshl_b32 s14, s13, 2
	s_add_i32 s14, s14, 0x20400
	v_mov_b32_e32 v6, s14
	ds_read_b32 v6, v6
	s_waitcnt lgkmcnt(0)
	v_readfirstlane_b32 s14, v6
	s_ashr_i32 s15, s14, 16
	s_lshl_b32 s13, s15, 2
	s_add_i32 s13, s13, 0x21600
	v_mov_b32_e32 v7, s13
	ds_read_b32 v7, v7
	s_and_b32 s14, s14, 0xffff
	s_lshl_b32 s14, s14, 8
	v_or_b32_e32 v8, s14, v4
	s_mul_i32 s15, s15, 0x8800
	v_add_lshl_u32 v9, v8, s15, 2
	s_waitcnt lgkmcnt(0)
	v_cmp_lt_i32_e32 vcc, v8, v7
	s_and_saveexec_b64 s[16:17], vcc
	global_load_dword v17, v9, s[4:5]
	s_or_b64 exec, exec, s[16:17]
	s_branch .Lmrb_nx7
.Lmrb_sh7:
	s_sub_i32 s14, s13, s20
	s_lshl_b32 s14, s14, 8
	v_or_b32_e32 v17, s14, v4
.Lmrb_nx7:
	s_add_i32 s10, s10, s12
.Lmrb_ld_done:
	s_waitcnt vmcnt(0)
	s_cmp_ge_i32 s11, s21
	s_cbranch_scc1 .Lmrb_wr_done
	ds_write_b32 v5, v10
	s_add_i32 s11, s11, s12
	s_cmp_ge_i32 s11, s21
	s_cbranch_scc1 .Lmrb_wr_done
	ds_write_b32 v5, v11 offset:2048
	s_add_i32 s11, s11, s12
	s_cmp_ge_i32 s11, s21
	s_cbranch_scc1 .Lmrb_wr_done
	ds_write_b32 v5, v12 offset:4096
	s_add_i32 s11, s11, s12
	s_cmp_ge_i32 s11, s21
	s_cbranch_scc1 .Lmrb_wr_done
	ds_write_b32 v5, v13 offset:6144
	s_add_i32 s11, s11, s12
	s_cmp_ge_i32 s11, s21
	s_cbranch_scc1 .Lmrb_wr_done
	ds_write_b32 v5, v14 offset:8192
	s_add_i32 s11, s11, s12
	s_cmp_ge_i32 s11, s21
	s_cbranch_scc1 .Lmrb_wr_done
	ds_write_b32 v5, v15 offset:10240
	s_add_i32 s11, s11, s12
	s_cmp_ge_i32 s11, s21
	s_cbranch_scc1 .Lmrb_wr_done
	ds_write_b32 v5, v16 offset:12288
	s_add_i32 s11, s11, s12
	s_cmp_ge_i32 s11, s21
	s_cbranch_scc1 .Lmrb_wr_done
	ds_write_b32 v5, v17 offset:14336
	s_add_i32 s11, s11, s12
.Lmrb_wr_done:
.LBB0_1615:
	s_or_b64 exec, exec, s[2:3]
	v_mov_b32_e32 v2, v0
	s_waitcnt lgkmcnt(0)
	s_barrier
	s_cmp_ge_i32 s71, s21
	v_readfirstlane_b32 s12, v2
	s_cbranch_scc1 .LBB0_1641
	s_lshr_b32 s2, s71, 31
	s_add_i32 s2, s71, s2
	s_ashr_i32 s58, s2, 1
	s_and_b32 s2, s2, -2
	s_sub_i32 s57, s71, s2
	s_cmp_ge_i32 s58, s20
	s_cbranch_scc0 .LBB0_1618
	s_lshl_b32 s2, s57, 19
	s_add_i32 s59, s2, 0x1200000
	s_cbranch_execz .LBB0_1619
	s_branch .LBB0_1620
